# rb-skip + selected-branch DMA issue spread over the tile group (scalar-base form) + top-k iteration without vcc round trips
# speedup vs baseline: 1.0187x; 1.0187x over previous
; #define DPP_I(x, ctrl) __builtin_amdgcn_update_dpp((int)(x), (int)(x), (ctrl), 0xF, 0xF, true)
; __device__ __forceinline__ void ph_attn_fast2(const Args& a, LAS unsigned char* lds) {
;     ...
;                     for (int it = 0; it < nsel - nforced; ++it) {
;                         int bv = max(max(max(vi[0], vi[1]), max(vi[2], vi[3])), max(max(vi[4], vi[5]), max(vi[6], vi[7])));
;                         bv = max(bv, DPP_I(bv, 0xB1)); bv = max(bv, DPP_I(bv, 0x4E)); bv = max(bv, DPP_I(bv, 0x141)); bv = max(bv, DPP_I(bv, 0x140));
;                         int bi = 255;
; #pragma unroll
;                         for (int k = 7; k >= 0; --k) bi = (vi[k] == bv) ? (li + 16 * k) : bi;
;                         bi = min(bi, DPP_I(bi, 0xB1)); bi = min(bi, DPP_I(bi, 0x4E)); bi = min(bi, DPP_I(bi, 0x141)); bi = min(bi, DPP_I(bi, 0x140));
;                         const unsigned bit = 1u << (bi & 31); const int wsel = bi >> 5;
;                         mm[0] |= (wsel == 0) ? bit : 0u; mm[1] |= (wsel == 1) ? bit : 0u; mm[2] |= (wsel == 2) ? bit : 0u; mm[3] |= (wsel == 3) ? bit : 0u;
;                         if ((bi & 15) == li) {
; #pragma unroll
;                             for (int k = 0; k < 8; ++k) if ((bi >> 4) == k) vi[k] = (int)0xFF800000;
;                         }
;                     }
.LBB0_2002:
	v_max3_i32 v19, v11, v2, v14
	v_max3_i32 v20, v12, v16, v15
	v_max3_i32 v19, v18, v17, v19
	v_max_i32_e32 v19, v19, v20
	s_nop 1
	v_max_i32_dpp v19, v19, v19 quad_perm:[1,0,3,2] row_mask:0xf bank_mask:0xf bound_ctrl:1
	s_nop 1
	v_max_i32_dpp v19, v19, v19 quad_perm:[2,3,0,1] row_mask:0xf bank_mask:0xf bound_ctrl:1
	s_nop 1
	v_max_i32_dpp v19, v19, v19 row_half_mirror row_mask:0xf bank_mask:0xf bound_ctrl:1
	s_nop 1
	v_max_i32_dpp v19, v19, v19 row_mirror row_mask:0xf bank_mask:0xf bound_ctrl:1
	v_cmp_eq_u32_e64 s[32:33], v17, v19
	v_cmp_eq_u32_e64 s[98:99], v18, v19
	v_cmp_eq_u32_e64 s[100:101], v15, v19
	v_cndmask_b32_e64 v20, v247, v240, s[32:33]
	v_cmp_eq_u32_e64 s[32:33], v16, v19
	v_cndmask_b32_e64 v20, v20, v238, s[98:99]
	v_cmp_eq_u32_e64 s[98:99], v12, v19
	v_cndmask_b32_e64 v20, v20, v236, s[100:101]
	v_cmp_eq_u32_e64 s[100:101], v14, v19
	v_cndmask_b32_e64 v20, v20, v234, s[32:33]
	v_cmp_eq_u32_e64 s[32:33], v2, v19
	v_cndmask_b32_e64 v20, v20, v232, s[98:99]
	v_cmp_eq_u32_e64 s[98:99], v11, v19
	v_cndmask_b32_e64 v20, v20, v230, s[100:101]
	v_cndmask_b32_e64 v20, v20, v228, s[32:33]
	v_cndmask_b32_e64 v19, v20, v211, s[98:99]
	s_nop 1
	v_min_i32_dpp v19, v19, v19 quad_perm:[1,0,3,2] row_mask:0xf bank_mask:0xf bound_ctrl:1
	s_nop 1
	v_min_i32_dpp v19, v19, v19 quad_perm:[2,3,0,1] row_mask:0xf bank_mask:0xf bound_ctrl:1
	s_nop 1
	v_min_i32_dpp v19, v19, v19 row_half_mirror row_mask:0xf bank_mask:0xf bound_ctrl:1
	s_nop 1
	v_min_i32_dpp v19, v19, v19 row_mirror row_mask:0xf bank_mask:0xf bound_ctrl:1
	v_cmp_eq_u32_e64 s[32:33], v19, v211
	v_cmp_eq_u32_e64 s[98:99], v19, v228
	v_cmp_eq_u32_e64 s[100:101], v19, v230
	v_cndmask_b32_e64 v11, v11, v246, s[32:33]
	v_cmp_eq_u32_e64 s[32:33], v19, v232
	v_cndmask_b32_e64 v2, v2, v246, s[98:99]
	v_cmp_eq_u32_e64 s[98:99], v19, v234
	v_cndmask_b32_e64 v14, v14, v246, s[100:101]
	v_cmp_eq_u32_e64 s[100:101], v19, v236
	v_cndmask_b32_e64 v12, v12, v246, s[32:33]
	v_cmp_eq_u32_e64 s[32:33], v19, v238
	v_cndmask_b32_e64 v16, v16, v246, s[98:99]
	v_cmp_eq_u32_e64 s[98:99], v19, v240
	v_cndmask_b32_e64 v15, v15, v246, s[100:101]
	v_lshlrev_b32_e64 v20, v19, 1
	v_cndmask_b32_e64 v18, v18, v246, s[32:33]
	v_ashrrev_i32_e32 v21, 5, v19
	v_cndmask_b32_e64 v17, v17, v246, s[98:99]
	v_cmp_gt_u32_e64 s[32:33], 32, v19
	v_cmp_eq_u32_e64 s[98:99], 1, v21
	v_cmp_eq_u32_e64 s[100:101], 2, v21
	v_cndmask_b32_e64 v22, 0, v20, s[32:33]
	v_cmp_eq_u32_e64 s[32:33], 3, v21
	v_cndmask_b32_e64 v23, 0, v20, s[98:99]
	v_or_b32_e32 v10, v22, v10
	v_cndmask_b32_e64 v24, 0, v20, s[100:101]
	v_or_b32_e32 v4, v23, v4
	v_cndmask_b32_e64 v25, 0, v20, s[32:33]
	v_or_b32_e32 v5, v24, v5
	v_or_b32_e32 v13, v25, v13
	s_add_i32 s26, s26, 1
	s_cmp_ge_i32 s26, s30
	s_cbranch_scc0 .LBB0_2002

; #define LAS __attribute__((address_space(3)))
; __device__ __forceinline__ void attn_qk2m(LAS unsigned char* Kb, const bf16x8 (&q)[2][2], int fr, int g4, const float (&cinit)[2], f32x4 (&s)[2][4]) {
;     bf16x8 kf[4][2];
; #pragma unroll
;     for (int c = 0; c < 4; ++c)
; #pragma unroll
;         for (int ks = 0; ks < 2; ++ks) kf[c][ks] = *(const LAS bf16x8*)(Kb + pg8::lds_byte(16 * c + fr, 32 * ks + 8 * g4));
;     __builtin_amdgcn_sched_barrier(0);
;     f32x4 ci[2];
; #pragma unroll
;     for (int rb = 0; rb < 2; ++rb) ci[rb] = (f32x4){cinit[rb], cinit[rb], cinit[rb], cinit[rb]};
; #pragma unroll
;     for (int c = 0; c < 4; ++c) {
; #pragma unroll
;         for (int ks = 0; ks < 2; ++ks) {
; #pragma unroll
;             for (int rb = 0; rb < 2; ++rb) s[rb][c] = __builtin_amdgcn_mfma_f32_16x16x32_bf16(kf[c][ks], q[rb][ks], ks == 0 ? ci[rb] : s[rb][c], 0, 0, 0);
;         }
;     }
; }
; __device__ __forceinline__ void ph_attn_fast2(const Args& a, LAS unsigned char* lds) {
;     ...
; #pragma unroll
;                 for (int i = 0; i < 4; ++i) if (i < nt_) AT_DMA(1, i, i);
;                 __syncthreads();
.LBB0_2079:
	s_add_i32 s33, s77, -3
	s_lshr_b32 s0, s33, 3
	s_and_b32 s0, s0, 0x1ffffffc
	v_add_u32_e32 v1, s0, v225
	ds_read2_b32 v[4:5], v1 offset1:16
	s_and_b32 s76, s33, 4
	s_add_i32 s5, s77, 4
	v_readlane_b32 s32, v252, 28
	s_cmp_eq_u32 s76, 0
	s_cselect_b32 s0, 0x10000, 0
	s_add_i32 s32, s32, s0
	s_add_i32 s0, s77, 1
	s_cmp_gt_u32 s0, s83
	s_cbranch_scc1 .Lslc_nm_dma_skip_0
	s_add_u32 s80, s74, 0x1fb08000
	s_addc_u32 s81, s75, 0
	s_add_i32 m0, s32, 0x0
	s_nop 0
	global_load_lds_dwordx4 v150, s[80:81]
	s_add_u32 s0, s74, 0x20b08000
	s_addc_u32 s1, s75, 0
	s_add_i32 m0, s32, 0x8000
	s_nop 0
	global_load_lds_dwordx4 v152, s[0:1]
.Lslc_nm_dma_skip_0:
.LBB0_2087:
	s_and_b32 s0, s33, 28
	s_lshl_b32 s0, 1, s0
	s_waitcnt lgkmcnt(0)
	v_and_b32_e32 v1, s0, v4
	v_cmp_ne_u32_e32 vcc, 0, v1
	v_and_b32_e32 v1, s0, v5
	v_cmp_ne_u32_e64 s[0:1], 0, v1
	s_add_i32 s78, s2, s77
	s_or_b64 s[80:81], vcc, s[0:1]
	s_cmp_eq_u64 s[80:81], 0
	s_cbranch_scc1 .LBB0_2093
	s_cmp_eq_u64 vcc, 0
	s_cbranch_scc1 .Lslc_nm_rb1_t0
	s_cmp_eq_u64 s[0:1], 0
	s_cbranch_scc1 .Lslc_nm_rb0_t0
	v_lshl_add_u32 v1, s76, 14, v220
	ds_read_b128 v[66:69], v1
	ds_read_b128 v[70:73], v1 offset:1024
	ds_read_b128 v[78:81], v1 offset:2048
	ds_read_b128 v[82:85], v1 offset:3072
	ds_read_b128 v[86:89], v1 offset:4096
	ds_read_b128 v[98:101], v1 offset:5120
	ds_read_b128 v[102:105], v1 offset:6144
	ds_read_b128 v[110:113], v1 offset:7168
	v_cndmask_b32_e64 v114, v248, 0, vcc
	v_cndmask_b32_e64 v118, v248, 0, s[0:1]
	v_mov_b32_e32 v115, v114
	v_mov_b32_e32 v116, v114
	v_mov_b32_e32 v117, v114
	v_mov_b32_e32 v119, v118
	v_mov_b32_e32 v120, v118
	v_mov_b32_e32 v121, v118
	s_waitcnt lgkmcnt(0)
	v_mfma_f32_16x16x32_bf16 v[74:77], v[66:69], v[10:13], v[114:117]
	s_cmp_lg_u32 s78, 3
	v_mfma_f32_16x16x32_bf16 v[66:69], v[66:69], v[18:21], v[118:121]
	v_mfma_f32_16x16x32_bf16 v[94:97], v[70:73], v[14:17], v[74:77]
	v_mfma_f32_16x16x32_bf16 v[74:77], v[70:73], v[22:25], v[66:69]
	v_mfma_f32_16x16x32_bf16 v[66:69], v[78:81], v[10:13], v[114:117]
	v_mfma_f32_16x16x32_bf16 v[70:73], v[78:81], v[18:21], v[118:121]
	v_mfma_f32_16x16x32_bf16 v[90:93], v[82:85], v[14:17], v[66:69]
	v_mfma_f32_16x16x32_bf16 v[66:69], v[86:89], v[10:13], v[114:117]
	v_mfma_f32_16x16x32_bf16 v[78:81], v[86:89], v[18:21], v[118:121]
	v_mfma_f32_16x16x32_bf16 v[86:89], v[98:101], v[14:17], v[66:69]
	v_mfma_f32_16x16x32_bf16 v[66:69], v[98:101], v[22:25], v[78:81]
	v_mfma_f32_16x16x32_bf16 v[78:81], v[102:105], v[10:13], v[114:117]
	v_mfma_f32_16x16x32_bf16 v[98:101], v[102:105], v[18:21], v[118:121]
	v_mfma_f32_16x16x32_bf16 v[70:73], v[82:85], v[22:25], v[70:73]
	v_mfma_f32_16x16x32_bf16 v[82:85], v[110:113], v[14:17], v[78:81]
	v_mfma_f32_16x16x32_bf16 v[78:81], v[110:113], v[22:25], v[98:101]
	s_cbranch_scc1 .LBB0_2092
	v_mov_b32_e32 v2, s96
	s_nop 5
	v_cndmask_b32_e64 v78, v78, v2, s[66:67]
	v_cndmask_b32_e64 v79, v79, v246, s[68:69]
	v_cndmask_b32_e64 v80, v80, v246, s[70:71]
	s_and_saveexec_b64 s[0:1], s[72:73]
	v_mov_b32_e32 v81, s96
	s_or_b64 exec, exec, s[0:1]
	v_mov_b32_e32 v2, s96
	v_cndmask_b32_e64 v1, v94, v2, s[8:9]
	v_cndmask_b32_e64 v94, v1, v94, s[10:11]
	v_cndmask_b32_e64 v1, v74, v2, s[42:43]
	v_cndmask_b32_e64 v95, v246, v95, s[10:11]
	v_cndmask_b32_e64 v96, v96, v246, s[12:13]
	v_cndmask_b32_e64 v97, v97, v246, s[14:15]
	v_cndmask_b32_e64 v90, v90, v2, s[16:17]
	v_cndmask_b32_e64 v91, v91, v246, s[18:19]
	v_cndmask_b32_e64 v92, v92, v246, s[20:21]
	v_cndmask_b32_e64 v93, v93, v246, s[22:23]
	v_cndmask_b32_e64 v86, v86, v2, s[24:25]
	v_cndmask_b32_e64 v87, v87, v246, s[26:27]
	v_cndmask_b32_e64 v88, v88, v246, s[28:29]
	v_cndmask_b32_e64 v89, v89, v246, s[30:31]
	v_cndmask_b32_e64 v82, v82, v2, s[34:35]
	v_cndmask_b32_e64 v83, v83, v246, s[36:37]
	v_cndmask_b32_e64 v84, v84, v246, s[38:39]
	v_cndmask_b32_e64 v85, v85, v246, s[40:41]
	v_cndmask_b32_e64 v75, v246, v75, s[44:45]
	v_cndmask_b32_e64 v74, v1, v74, s[44:45]
	v_cndmask_b32_e64 v76, v76, v246, s[46:47]
	v_cndmask_b32_e64 v77, v77, v246, s[48:49]
	v_cndmask_b32_e64 v70, v70, v2, s[50:51]
	v_cndmask_b32_e64 v71, v71, v246, s[52:53]
	v_cndmask_b32_e64 v72, v72, v246, s[54:55]
	v_cndmask_b32_e64 v73, v73, v246, s[56:57]
	v_cndmask_b32_e64 v66, v66, v2, s[58:59]
	v_cndmask_b32_e64 v67, v67, v246, s[60:61]
	v_cndmask_b32_e64 v68, v68, v246, s[62:63]
	v_cndmask_b32_e64 v69, v69, v246, s[64:65]

.LBB0_2093:
	s_add_i32 s0, s77, 2
	s_cmp_gt_u32 s0, s83
	s_cbranch_scc1 .Lslc_nm_dma_skip_1
	s_add_u32 s80, s74, 0x1fb0a000
	s_addc_u32 s81, s75, 0
	s_add_i32 m0, s32, 0x2000
	s_nop 0
	global_load_lds_dwordx4 v150, s[80:81]
	s_add_u32 s0, s74, 0x20b0a000
	s_addc_u32 s1, s75, 0
	s_add_i32 m0, s32, 0xa000
	s_nop 0
	global_load_lds_dwordx4 v152, s[0:1]

.LBB0_2101:
	s_add_i32 s0, s77, 3
	s_cmp_gt_u32 s0, s83
	s_cbranch_scc1 .Lslc_nm_dma_skip_2
	s_add_u32 s80, s74, 0x1fb0c000
	s_addc_u32 s81, s75, 0
	s_add_i32 m0, s32, 0x4000
	s_nop 0
	global_load_lds_dwordx4 v150, s[80:81]
	s_add_u32 s0, s74, 0x20b0c000
	s_addc_u32 s1, s75, 0
	s_add_i32 m0, s32, 0xc000
	s_nop 0
	global_load_lds_dwordx4 v152, s[0:1]

.LBB0_2108:
	s_add_i32 s0, s77, 4
	s_cmp_gt_u32 s0, s83
	s_cbranch_scc1 .Lslc_nm_dma_skip_3
	s_add_u32 s80, s74, 0x1fb0e000
	s_addc_u32 s81, s75, 0
	s_add_i32 m0, s32, 0x6000
	s_nop 0
	global_load_lds_dwordx4 v150, s[80:81]
	s_add_u32 s0, s74, 0x20b0e000
	s_addc_u32 s1, s75, 0
	s_add_i32 m0, s32, 0xe000
	s_nop 0
	global_load_lds_dwordx4 v152, s[0:1]

; __global__ void __launch_bounds__(512, 2) fwd_kernel(Args a) {
	.amdhsa_kernel _Z10fwd_kernel4Args
		.amdhsa_group_segment_fixed_size 0
		.amdhsa_private_segment_fixed_size 0
		.amdhsa_kernarg_size 544
		.amdhsa_user_sgpr_count 2
		.amdhsa_user_sgpr_dispatch_ptr 0
		.amdhsa_user_sgpr_queue_ptr 0
		.amdhsa_user_sgpr_kernarg_segment_ptr 1
		.amdhsa_user_sgpr_dispatch_id 0
		.amdhsa_user_sgpr_kernarg_preload_length 0
		.amdhsa_user_sgpr_kernarg_preload_offset 0
		.amdhsa_user_sgpr_private_segment_size 0
		.amdhsa_uses_dynamic_stack 0
		.amdhsa_enable_private_segment 0
		.amdhsa_system_sgpr_workgroup_id_x 1
		.amdhsa_system_sgpr_workgroup_id_y 0
		.amdhsa_system_sgpr_workgroup_id_z 0
		.amdhsa_system_sgpr_workgroup_info 0
		.amdhsa_system_vgpr_workitem_id 0
		.amdhsa_next_free_vgpr 253
		.amdhsa_next_free_sgpr 102
		.amdhsa_accum_offset 256
		.amdhsa_reserve_vcc 1
		.amdhsa_float_round_mode_32 0
		.amdhsa_float_round_mode_16_64 0
		.amdhsa_float_denorm_mode_32 3
		.amdhsa_float_denorm_mode_16_64 3
		.amdhsa_dx10_clamp 1
		.amdhsa_ieee_mode 1
		.amdhsa_fp16_overflow 0
		.amdhsa_tg_split 0
		.amdhsa_exception_fp_ieee_invalid_op 0
		.amdhsa_exception_fp_denorm_src 0
		.amdhsa_exception_fp_ieee_div_zero 0
		.amdhsa_exception_fp_ieee_overflow 0
		.amdhsa_exception_fp_ieee_underflow 0
		.amdhsa_exception_fp_ieee_inexact 0
		.amdhsa_exception_int_div_zero 0
	.end_amdhsa_kernel

; __global__ void __launch_bounds__(512, 2) fwd_kernel(Args a) {
amdhsa.kernels:
  - .agpr_count:     0
    .args:
      - .offset:         0
        .size:           288
        .value_kind:     by_value
      - .offset:         288
        .size:           4
        .value_kind:     hidden_block_count_x
      - .offset:         292
        .size:           4
        .value_kind:     hidden_block_count_y
      - .offset:         296
        .size:           4
        .value_kind:     hidden_block_count_z
      - .offset:         300
        .size:           2
        .value_kind:     hidden_group_size_x
      - .offset:         302
        .size:           2
        .value_kind:     hidden_group_size_y
      - .offset:         304
        .size:           2
        .value_kind:     hidden_group_size_z
      - .offset:         306
        .size:           2
        .value_kind:     hidden_remainder_x
      - .offset:         308
        .size:           2
        .value_kind:     hidden_remainder_y
      - .offset:         310
        .size:           2
        .value_kind:     hidden_remainder_z
      - .offset:         328
        .size:           8
        .value_kind:     hidden_global_offset_x
      - .offset:         336
        .size:           8
        .value_kind:     hidden_global_offset_y
      - .offset:         344
        .size:           8
        .value_kind:     hidden_global_offset_z
      - .offset:         352
        .size:           2
        .value_kind:     hidden_grid_dims
      - .offset:         408
        .size:           4
        .value_kind:     hidden_dynamic_lds_size
    .group_segment_fixed_size: 0
    .kernarg_segment_align: 8
    .kernarg_segment_size: 544
    .language:       OpenCL C
    .language_version:
      - 2
      - 0
    .max_flat_workgroup_size: 512
    .name:           _Z10fwd_kernel4Args
    .private_segment_fixed_size: 0
    .sgpr_count:     108
    .sgpr_spill_count: 129
    .symbol:         _Z10fwd_kernel4Args.kd
    .uniform_work_group_size: 1
    .uses_dynamic_stack: false
    .vgpr_count:     253
    .vgpr_spill_count: 0
    .wavefront_size: 64
